# phase-7 residual epilogue: X loads batched 16 in flight with counted vmcnt instead of one load per vmcnt(0)
# baseline (speedup 1.0000x reference)
;     __device__ __forceinline__ void operator()(const f32x4 (&acc)[2][2][4][2], const Unit& u, int wr, int wc, int fr, int fq) const {
;         const int row0 = u.pm * BM + wr * 64 + fr, col0 = u.pn * BM + wc * 32 + 4 * fq;
;         f32x4 gv[2][2];
; #pragma unroll
;         for (int bj = 0; bj < 2; ++bj)
; #pragma unroll
;             for (int n = 0; n < 2; ++n) gv[bj][n] = *(const f32x4*)(gate + col0 + bj * HALF + n * 16);
; #pragma unroll
;         for (int ai = 0; ai < 2; ++ai)
; #pragma unroll
;             for (int m = 0; m < 4; ++m) { const int row = row0 + ai * HALF + m * 16;
; #pragma unroll
;                 for (int bj = 0; bj < 2; ++bj)
; #pragma unroll
;                     for (int n = 0; n < 2; ++n) { const size_t off = (size_t)row * 2048 + col0 + bj * HALF + n * 16;
;                         *(f32x4*)(O + off) = *(const f32x4*)(X + off) + gv[bj][n] * acc[ai][bj][m][n]; } }
;     }
.LBB0_863:
	v_lshl_add_u32 v174, s46, 8, v164
	v_lshl_or_b32 v162, s5, 8, v166
	v_ashrrev_i32_e32 v175, 31, v174
	v_ashrrev_i32_e32 v163, 31, v162
	v_lshlrev_b64 v[130:131], 11, v[174:175]
	v_lshl_add_u64 v[130:131], v[130:131], 0, v[162:163]
	v_lshlrev_b64 v[160:161], 2, v[130:131]
	v_lshl_add_u64 v[128:129], v[162:163], 2, s[10:11]
	v_lshl_add_u64 v[176:177], s[2:3], 0, v[160:161]
	v_lshl_add_u64 v[158:159], s[8:9], 0, v[160:161]
	s_mov_b64 s[48:49], 0x20000
	s_mov_b64 s[50:51], 0x40000
	s_mov_b64 s[52:53], 0x60000
	global_load_dwordx4 v[140:143], v[128:129], off
	global_load_dwordx4 v[136:139], v[128:129], off offset:64
	global_load_dwordx4 v[132:135], v[128:129], off offset:512
	s_nop 0
	global_load_dwordx4 v[128:131], v[128:129], off offset:576
	global_load_dwordx4 v[178:181], v[176:177], off
	global_load_dwordx4 v[182:185], v[176:177], off offset:64
	global_load_dwordx4 v[186:189], v[176:177], off offset:512
	global_load_dwordx4 v[190:193], v[176:177], off offset:576
	v_lshl_add_u64 v[170:171], v[176:177], 0, s[48:49]
	global_load_dwordx4 v[194:197], v[170:171], off
	global_load_dwordx4 v[198:201], v[170:171], off offset:64
	global_load_dwordx4 v[202:205], v[170:171], off offset:512
	global_load_dwordx4 v[206:209], v[170:171], off offset:576
	v_lshl_add_u64 v[162:163], v[176:177], 0, s[50:51]
	global_load_dwordx4 v[210:213], v[162:163], off
	global_load_dwordx4 v[214:217], v[162:163], off offset:64
	global_load_dwordx4 v[218:221], v[162:163], off offset:512
	global_load_dwordx4 v[222:225], v[162:163], off offset:576
	v_lshl_add_u64 v[170:171], v[176:177], 0, s[52:53]
	global_load_dwordx4 v[226:229], v[170:171], off
	global_load_dwordx4 v[230:233], v[170:171], off offset:64
	global_load_dwordx4 v[234:237], v[170:171], off offset:512
	global_load_dwordx4 v[238:241], v[170:171], off offset:576
	s_waitcnt vmcnt(8)
	v_pk_fma_f32 v[126:127], v[126:127], v[142:143], v[180:181]
	v_pk_fma_f32 v[124:125], v[124:125], v[140:141], v[178:179]
	global_store_dwordx4 v[158:159], v[124:127], off
	v_pk_fma_f32 v[122:123], v[122:123], v[138:139], v[184:185]
	v_pk_fma_f32 v[120:121], v[120:121], v[136:137], v[182:183]
	global_store_dwordx4 v[158:159], v[120:123], off offset:64
	v_pk_fma_f32 v[118:119], v[118:119], v[134:135], v[188:189]
	v_pk_fma_f32 v[116:117], v[116:117], v[132:133], v[186:187]
	global_store_dwordx4 v[158:159], v[116:119], off offset:512
	v_pk_fma_f32 v[110:111], v[110:111], v[130:131], v[192:193]
	v_pk_fma_f32 v[108:109], v[108:109], v[128:129], v[190:191]
	global_store_dwordx4 v[158:159], v[108:111], off offset:576
	v_lshl_add_u64 v[174:175], v[158:159], 0, s[48:49]
	v_pk_fma_f32 v[114:115], v[114:115], v[142:143], v[196:197]
	v_pk_fma_f32 v[112:113], v[112:113], v[140:141], v[194:195]
	global_store_dwordx4 v[174:175], v[112:115], off
	v_pk_fma_f32 v[106:107], v[106:107], v[138:139], v[200:201]
	v_pk_fma_f32 v[104:105], v[104:105], v[136:137], v[198:199]
	global_store_dwordx4 v[174:175], v[104:107], off offset:64
	v_pk_fma_f32 v[102:103], v[102:103], v[134:135], v[204:205]
	v_pk_fma_f32 v[100:101], v[100:101], v[132:133], v[202:203]
	global_store_dwordx4 v[174:175], v[100:103], off offset:512
	v_pk_fma_f32 v[94:95], v[94:95], v[130:131], v[208:209]
	v_pk_fma_f32 v[92:93], v[92:93], v[128:129], v[206:207]
	global_store_dwordx4 v[174:175], v[92:95], off offset:576
	v_lshl_add_u64 v[162:163], v[176:177], 0, s[26:27]
	global_load_dwordx4 v[178:181], v[162:163], off
	global_load_dwordx4 v[182:185], v[162:163], off offset:64
	global_load_dwordx4 v[186:189], v[162:163], off offset:512
	global_load_dwordx4 v[190:193], v[162:163], off offset:576
	v_lshl_add_u64 v[170:171], v[176:177], 0, s[28:29]
	global_load_dwordx4 v[194:197], v[170:171], off
	global_load_dwordx4 v[198:201], v[170:171], off offset:64
	global_load_dwordx4 v[202:205], v[170:171], off offset:512
	global_load_dwordx4 v[206:209], v[170:171], off offset:576
	s_waitcnt vmcnt(16)
;     __device__ __forceinline__ void operator()(const f32x4 (&acc)[2][2][4][2], const Unit& u, int wr, int wc, int fr, int fq) const {
;         const int row0 = u.pm * BM + wr * 64 + fr, col0 = u.pn * BM + wc * 32 + 4 * fq;
;         f32x4 gv[2][2];
; #pragma unroll
;         for (int bj = 0; bj < 2; ++bj)
; #pragma unroll
;             for (int n = 0; n < 2; ++n) gv[bj][n] = *(const f32x4*)(gate + col0 + bj * HALF + n * 16);
; #pragma unroll
;         for (int ai = 0; ai < 2; ++ai)
; #pragma unroll
;             for (int m = 0; m < 4; ++m) { const int row = row0 + ai * HALF + m * 16;
; #pragma unroll
;                 for (int bj = 0; bj < 2; ++bj)
; #pragma unroll
;                     for (int n = 0; n < 2; ++n) { const size_t off = (size_t)row * 2048 + col0 + bj * HALF + n * 16;
;                         *(f32x4*)(O + off) = *(const f32x4*)(X + off) + gv[bj][n] * acc[ai][bj][m][n]; } }
;     }
	v_lshl_add_u64 v[172:173], v[158:159], 0, s[50:51]
	v_pk_fma_f32 v[98:99], v[98:99], v[142:143], v[212:213]
	v_pk_fma_f32 v[96:97], v[96:97], v[140:141], v[210:211]
	global_store_dwordx4 v[172:173], v[96:99], off
	v_pk_fma_f32 v[90:91], v[90:91], v[138:139], v[216:217]
	v_pk_fma_f32 v[88:89], v[88:89], v[136:137], v[214:215]
	global_store_dwordx4 v[172:173], v[88:91], off offset:64
	v_pk_fma_f32 v[86:87], v[86:87], v[134:135], v[220:221]
	v_pk_fma_f32 v[84:85], v[84:85], v[132:133], v[218:219]
	global_store_dwordx4 v[172:173], v[84:87], off offset:512
	v_pk_fma_f32 v[78:79], v[78:79], v[130:131], v[224:225]
	v_pk_fma_f32 v[76:77], v[76:77], v[128:129], v[222:223]
	global_store_dwordx4 v[172:173], v[76:79], off offset:576
	v_lshl_add_u64 v[174:175], v[158:159], 0, s[52:53]
	v_pk_fma_f32 v[82:83], v[82:83], v[142:143], v[228:229]
	v_pk_fma_f32 v[80:81], v[80:81], v[140:141], v[226:227]
	global_store_dwordx4 v[174:175], v[80:83], off
	v_pk_fma_f32 v[74:75], v[74:75], v[138:139], v[232:233]
	v_pk_fma_f32 v[72:73], v[72:73], v[136:137], v[230:231]
	global_store_dwordx4 v[174:175], v[72:75], off offset:64
	v_pk_fma_f32 v[70:71], v[70:71], v[134:135], v[236:237]
	v_pk_fma_f32 v[68:69], v[68:69], v[132:133], v[234:235]
	global_store_dwordx4 v[174:175], v[68:71], off offset:512
	v_pk_fma_f32 v[66:67], v[66:67], v[130:131], v[240:241]
	v_pk_fma_f32 v[64:65], v[64:65], v[128:129], v[238:239]
	global_store_dwordx4 v[174:175], v[64:67], off offset:576
	v_lshl_add_u64 v[162:163], v[176:177], 0, s[30:31]
	global_load_dwordx4 v[210:213], v[162:163], off
	global_load_dwordx4 v[214:217], v[162:163], off offset:64
	global_load_dwordx4 v[218:221], v[162:163], off offset:512
	global_load_dwordx4 v[222:225], v[162:163], off offset:576
	v_lshl_add_u64 v[170:171], v[176:177], 0, s[34:35]
	global_load_dwordx4 v[226:229], v[170:171], off
	global_load_dwordx4 v[230:233], v[170:171], off offset:64
	global_load_dwordx4 v[234:237], v[170:171], off offset:512
	global_load_dwordx4 v[238:241], v[170:171], off offset:576
	s_waitcnt vmcnt(16)
	v_lshl_add_u64 v[172:173], v[158:159], 0, s[26:27]
	v_pk_fma_f32 v[62:63], v[62:63], v[142:143], v[180:181]
	v_pk_fma_f32 v[60:61], v[60:61], v[140:141], v[178:179]
	global_store_dwordx4 v[172:173], v[60:63], off
	v_pk_fma_f32 v[58:59], v[58:59], v[138:139], v[184:185]
	v_pk_fma_f32 v[56:57], v[56:57], v[136:137], v[182:183]
	global_store_dwordx4 v[172:173], v[56:59], off offset:64
	v_pk_fma_f32 v[54:55], v[54:55], v[134:135], v[188:189]
	v_pk_fma_f32 v[52:53], v[52:53], v[132:133], v[186:187]
	global_store_dwordx4 v[172:173], v[52:55], off offset:512
	v_pk_fma_f32 v[46:47], v[46:47], v[130:131], v[192:193]
	v_pk_fma_f32 v[44:45], v[44:45], v[128:129], v[190:191]
	global_store_dwordx4 v[172:173], v[44:47], off offset:576
	v_lshl_add_u64 v[174:175], v[158:159], 0, s[28:29]
	v_pk_fma_f32 v[50:51], v[50:51], v[142:143], v[196:197]
	v_pk_fma_f32 v[48:49], v[48:49], v[140:141], v[194:195]
	global_store_dwordx4 v[174:175], v[48:51], off
	v_pk_fma_f32 v[42:43], v[42:43], v[138:139], v[200:201]
	v_pk_fma_f32 v[40:41], v[40:41], v[136:137], v[198:199]
	global_store_dwordx4 v[174:175], v[40:43], off offset:64
	v_pk_fma_f32 v[38:39], v[38:39], v[134:135], v[204:205]
	v_pk_fma_f32 v[36:37], v[36:37], v[132:133], v[202:203]
	global_store_dwordx4 v[174:175], v[36:39], off offset:512
	v_pk_fma_f32 v[30:31], v[30:31], v[130:131], v[208:209]
	v_pk_fma_f32 v[28:29], v[28:29], v[128:129], v[206:207]
	global_store_dwordx4 v[174:175], v[28:31], off offset:576
	s_waitcnt vmcnt(8)
	v_lshl_add_u64 v[172:173], v[158:159], 0, s[30:31]
	v_pk_fma_f32 v[34:35], v[34:35], v[142:143], v[212:213]
	v_pk_fma_f32 v[32:33], v[32:33], v[140:141], v[210:211]
	global_store_dwordx4 v[172:173], v[32:35], off
	v_pk_fma_f32 v[26:27], v[26:27], v[138:139], v[216:217]
	v_pk_fma_f32 v[24:25], v[24:25], v[136:137], v[214:215]
	global_store_dwordx4 v[172:173], v[24:27], off offset:64
	v_pk_fma_f32 v[22:23], v[22:23], v[134:135], v[220:221]
	v_pk_fma_f32 v[20:21], v[20:21], v[132:133], v[218:219]
	global_store_dwordx4 v[172:173], v[20:23], off offset:512
	v_pk_fma_f32 v[14:15], v[14:15], v[130:131], v[224:225]
	v_pk_fma_f32 v[12:13], v[12:13], v[128:129], v[222:223]
	global_store_dwordx4 v[172:173], v[12:15], off offset:576
	v_lshl_add_u64 v[174:175], v[158:159], 0, s[34:35]
	v_pk_fma_f32 v[18:19], v[18:19], v[142:143], v[228:229]
	v_pk_fma_f32 v[16:17], v[16:17], v[140:141], v[226:227]
	global_store_dwordx4 v[174:175], v[16:19], off
	v_pk_fma_f32 v[10:11], v[10:11], v[138:139], v[232:233]
	v_pk_fma_f32 v[8:9], v[8:9], v[136:137], v[230:231]
	global_store_dwordx4 v[174:175], v[8:11], off offset:64
	v_pk_fma_f32 v[6:7], v[6:7], v[134:135], v[236:237]
	v_pk_fma_f32 v[4:5], v[4:5], v[132:133], v[234:235]
	global_store_dwordx4 v[174:175], v[4:7], off offset:512
	v_pk_fma_f32 v[2:3], v[2:3], v[130:131], v[240:241]
	v_pk_fma_f32 v[0:1], v[0:1], v[128:129], v[238:239]
	global_store_dwordx4 v[174:175], v[0:3], off offset:576
	s_andn2_b64 vcc, exec, s[40:41]
	s_mov_b64 s[40:41], -1
	s_cbranch_vccnz .LBB0_851
	s_andn2_b64 vcc, exec, s[6:7]
	s_cbranch_vccnz .LBB0_850
	s_barrier
	s_branch .LBB0_850
